# selection bin edges bh/bl: 32-lane DPP scan + ballot over the crossing lane's bins instead of two 32-step serial chains (values checked identical)
# speedup vs baseline: 1.0123x; 1.0011x over previous
; #define LAS __attribute__((address_space(3)))
; #define LDS_WAIT() asm volatile("s_waitcnt lgkmcnt(0)" ::: "memory")
; __device__ __forceinline__ bool dsa2_sampled(LAS unsigned char* wl, const unsigned (&kk)[128], int nreg, int n, int lane) {
;     ...
;     for (int i = 0; i < 128; i += 8) { if (i < nreg) { const unsigned k = kk[i]; if (k != 0u) (void)__hip_atomic_fetch_add(&hist[k >> 21], 1u, __ATOMIC_RELAXED, __HIP_MEMORY_SCOPE_WORKGROUP); } }
;     LDS_WAIT();
;     unsigned hv[32]; unsigned mine = 0u;
; #pragma unroll
;     for (int i = 0; i < 8; ++i) { const v4u v = *(const LAS v4u*)(hist + lane * 32 + 4 * i); hv[4 * i] = v.x; hv[4 * i + 1] = v.y; hv[4 * i + 2] = v.z; hv[4 * i + 3] = v.w; mine += (v.x + v.y) + (v.z + v.w); }
.LBB0_734:
	s_or_b64 exec, exec, s[0:1]
	s_cmp_gt_u32 s49, 24
	s_cselect_b64 s[0:1], -1, 0
	v_cmp_ne_u32_e32 vcc, 0, v140
	s_and_b64 s[2:3], s[0:1], vcc
	s_and_saveexec_b64 s[0:1], s[2:3]
	v_lshrrev_b32_e32 v0, 19, v140
	v_and_b32_e32 v0, 0x1ffc, v0
	v_add_u32_e32 v0, s57, v0
	ds_add_u32 v0, v248
	s_or_b64 exec, exec, s[0:1]
	s_cmp_lt_u32 s49, 33
	s_cselect_b64 s[88:89], -1, 0
	s_cmp_gt_u32 s49, 32
	s_cselect_b64 s[0:1], -1, 0
	v_cmp_ne_u32_e32 vcc, 0, v135
	s_and_b64 s[2:3], s[0:1], vcc
	s_and_saveexec_b64 s[0:1], s[2:3]
	v_lshrrev_b32_e32 v0, 19, v135
	v_and_b32_e32 v0, 0x1ffc, v0
	v_add_u32_e32 v0, s57, v0
	ds_add_u32 v0, v248
	s_or_b64 exec, exec, s[0:1]
	s_cmp_gt_u32 s49, 40
	s_cselect_b64 s[0:1], -1, 0
	v_cmp_ne_u32_e32 vcc, 0, v121
	s_and_b64 s[2:3], s[0:1], vcc
	s_and_saveexec_b64 s[0:1], s[2:3]
	v_lshrrev_b32_e32 v0, 19, v121
	v_and_b32_e32 v0, 0x1ffc, v0
	v_add_u32_e32 v0, s57, v0
	ds_add_u32 v0, v248
	s_or_b64 exec, exec, s[0:1]
	s_cmp_lt_u32 s49, 49
	s_cselect_b64 s[86:87], -1, 0
	s_cmp_gt_u32 s49, 48
	s_cselect_b64 s[0:1], -1, 0
	v_cmp_ne_u32_e32 vcc, 0, v113
	s_and_b64 s[2:3], s[0:1], vcc
	s_and_saveexec_b64 s[0:1], s[2:3]
	v_lshrrev_b32_e32 v0, 19, v113
	v_and_b32_e32 v0, 0x1ffc, v0
	v_add_u32_e32 v0, s57, v0
	ds_add_u32 v0, v248
	s_or_b64 exec, exec, s[0:1]
	s_cmp_gt_u32 s49, 56
	s_cselect_b64 s[0:1], -1, 0
	v_cmp_ne_u32_e32 vcc, 0, v105
	s_and_b64 s[2:3], s[0:1], vcc
	s_and_saveexec_b64 s[0:1], s[2:3]
	v_lshrrev_b32_e32 v0, 19, v105
	v_and_b32_e32 v0, 0x1ffc, v0
	v_add_u32_e32 v0, s57, v0
	ds_add_u32 v0, v248
	s_or_b64 exec, exec, s[0:1]
	s_cmpk_lt_u32 s49, 0x41
	s_cselect_b64 s[84:85], -1, 0
	s_cmp_gt_u32 s49, 64
	s_cselect_b64 s[0:1], -1, 0
	v_cmp_ne_u32_e32 vcc, 0, v101
	s_and_b64 s[2:3], s[0:1], vcc
	s_and_saveexec_b64 s[0:1], s[2:3]
	v_lshrrev_b32_e32 v0, 19, v101
	v_and_b32_e32 v0, 0x1ffc, v0
	v_add_u32_e32 v0, s57, v0
	ds_add_u32 v0, v248
	s_or_b64 exec, exec, s[0:1]
	s_cmpk_gt_u32 s49, 0x48
	s_cselect_b64 s[0:1], -1, 0
	v_cmp_ne_u32_e32 vcc, 0, v89
	s_and_b64 s[2:3], s[0:1], vcc
	s_and_saveexec_b64 s[0:1], s[2:3]
	v_lshrrev_b32_e32 v0, 19, v89
	v_and_b32_e32 v0, 0x1ffc, v0
	v_add_u32_e32 v0, s57, v0
	ds_add_u32 v0, v248
	s_or_b64 exec, exec, s[0:1]
	s_cmpk_lt_u32 s49, 0x51
	s_cselect_b64 s[14:15], -1, 0
	s_cmpk_gt_u32 s49, 0x50
	s_cselect_b64 s[0:1], -1, 0
	v_cmp_ne_u32_e32 vcc, 0, v81
	s_and_b64 s[2:3], s[0:1], vcc
	s_and_saveexec_b64 s[0:1], s[2:3]
	v_lshrrev_b32_e32 v0, 19, v81
	v_and_b32_e32 v0, 0x1ffc, v0
	v_add_u32_e32 v0, s57, v0
	ds_add_u32 v0, v248
	s_or_b64 exec, exec, s[0:1]
	s_cmpk_gt_u32 s49, 0x58
	s_cselect_b64 s[0:1], -1, 0
	v_cmp_ne_u32_e32 vcc, 0, v73
	s_and_b64 s[2:3], s[0:1], vcc
	s_and_saveexec_b64 s[0:1], s[2:3]
	v_lshrrev_b32_e32 v0, 19, v73
	v_and_b32_e32 v0, 0x1ffc, v0
	v_add_u32_e32 v0, s57, v0
	ds_add_u32 v0, v248
	s_or_b64 exec, exec, s[0:1]
	s_cmpk_lt_u32 s49, 0x61
	s_cselect_b64 s[12:13], -1, 0
	s_cmpk_gt_u32 s49, 0x60
	s_cselect_b64 s[0:1], -1, 0
	v_cmp_ne_u32_e32 vcc, 0, v69
	s_and_b64 s[2:3], s[0:1], vcc
	s_and_saveexec_b64 s[0:1], s[2:3]
	v_lshrrev_b32_e32 v0, 19, v69
	v_and_b32_e32 v0, 0x1ffc, v0
	v_add_u32_e32 v0, s57, v0
	ds_add_u32 v0, v248
	s_or_b64 exec, exec, s[0:1]
	s_cmpk_gt_u32 s49, 0x68
	s_cselect_b64 s[0:1], -1, 0
	v_cmp_ne_u32_e32 vcc, 0, v58
	s_and_b64 s[2:3], s[0:1], vcc
	s_and_saveexec_b64 s[0:1], s[2:3]
	v_lshrrev_b32_e32 v0, 19, v58
	v_and_b32_e32 v0, 0x1ffc, v0
	v_add_u32_e32 v0, s57, v0
	ds_add_u32 v0, v248
	s_or_b64 exec, exec, s[0:1]
	s_cmpk_lt_u32 s49, 0x71
	s_cselect_b64 s[4:5], -1, 0
	s_cmpk_gt_u32 s49, 0x70
	s_cselect_b64 s[0:1], -1, 0
	v_cmp_ne_u32_e32 vcc, 0, v49
	s_and_b64 s[2:3], s[0:1], vcc
	s_and_saveexec_b64 s[0:1], s[2:3]
	v_lshrrev_b32_e32 v0, 19, v49
	v_and_b32_e32 v0, 0x1ffc, v0
	v_add_u32_e32 v0, s57, v0
	ds_add_u32 v0, v248
	s_or_b64 exec, exec, s[0:1]
	s_cmpk_gt_u32 s49, 0x78
	s_cselect_b64 s[0:1], -1, 0
	v_cmp_ne_u32_e32 vcc, 0, v41
	s_and_b64 s[2:3], s[0:1], vcc
	s_and_saveexec_b64 s[0:1], s[2:3]
	v_lshrrev_b32_e32 v0, 19, v41
	v_and_b32_e32 v0, 0x1ffc, v0
	v_add_u32_e32 v0, s57, v0
	ds_add_u32 v0, v248
	s_or_b64 exec, exec, s[0:1]
	s_waitcnt lgkmcnt(0)
	ds_read_b128 v[0:3], v167
	ds_read_b128 v[4:7], v167 offset:16
	ds_read_b128 v[8:11], v167 offset:32
	ds_read_b128 v[12:15], v167 offset:48
	ds_read_b128 v[16:19], v167 offset:64
	ds_read_b128 v[20:23], v167 offset:80
	s_waitcnt lgkmcnt(5)
	v_add_u32_e32 v0, v1, v0
	v_add3_u32 v0, v0, v3, v2
	s_waitcnt lgkmcnt(4)
; __device__ __forceinline__ int lane_op() { int l = (int)__builtin_amdgcn_mbcnt_hi(~0u, __builtin_amdgcn_mbcnt_lo(~0u, 0u)); asm volatile("" : "+v"(l)); return l; }
; #define SHI(v, s) bperm_((s), (v))
; __device__ __forceinline__ bool dsa2_sampled(LAS unsigned char* wl, const unsigned (&kk)[128], int nreg, int n, int lane) {
;     ...
;     const unsigned pre_ = dpp_scan_add_u32(mine); const unsigned incl = (unsigned)__builtin_amdgcn_readlane((int)pre_, 63) - pre_ + mine; const int lop_ = lane_op(); (void)lop_;
;     const unsigned above = incl - mine; const unsigned ns = SHI(incl, 0);
;     const float E = (float)ns * 256.f / (float)n, mg = 3.f * sqrtf(E) + 3.f;
;     const int rhi = (int)fmaxf(E - mg, 0.f), rlo = (int)(E + mg) + 1;
;     int bhl = -1, bll = -1; { unsigned s = above;
; #pragma unroll
;         for (int i = 31; i >= 0; --i) { if ((int)s <= rhi) bhl = i; s += hv[i]; if (bll < 0 && (int)s >= rlo) bll = i; } }
;     const bool hasH = ((int)above <= rhi) && ((int)incl > rhi || lane == 0), hasL = ((int)incl >= rlo) && ((int)above < rlo);
;     const unsigned long long mH = __ballot(hasH), mL = __ballot(hasL);
;     if (mH == 0ull) return false;
;     const int sH = 63 - __builtin_clzll(mH);
;     const unsigned bh = (unsigned)SHI(lane * 32 + (bhl < 0 ? 0 : bhl), sH);
;     unsigned bl = 1u; if (mL != 0ull) { const int sL = 63 - __builtin_clzll(mL); bl = (unsigned)SHI(lane * 32 + (bll < 0 ? 0 : bll), sL); }
;     bl = bl < 1u ? 1u : bl; if (bl > bh) bl = bh;
	v_add3_u32 v0, v0, v5, v4
	v_add3_u32 v0, v0, v7, v6
	s_waitcnt lgkmcnt(3)
	v_add3_u32 v0, v0, v9, v8
	v_add3_u32 v0, v0, v11, v10
	s_waitcnt lgkmcnt(2)
	v_add3_u32 v0, v0, v13, v12
	v_add3_u32 v0, v0, v15, v14
	ds_read_b128 v[24:27], v167 offset:96
	ds_read_b128 v[28:31], v167 offset:112
	s_waitcnt lgkmcnt(3)
	v_add3_u32 v0, v0, v17, v16
	v_add3_u32 v0, v0, v19, v18
	s_waitcnt lgkmcnt(2)
	v_add3_u32 v0, v0, v21, v20
	v_add3_u32 v0, v0, v23, v22
	s_waitcnt lgkmcnt(1)
	v_add3_u32 v0, v0, v25, v24
	v_add3_u32 v0, v0, v27, v26
	s_waitcnt lgkmcnt(0)
	v_add3_u32 v0, v0, v29, v28
	v_add3_u32 v0, v0, v31, v30
	s_add_i32 s0, s58, 1
	v_cvt_f32_i32_e32 v169, s0
	v_add_u32_dpp v168, v0, v0 row_shr:1 row_mask:0xf bank_mask:0xf bound_ctrl:1
	v_cmp_eq_u32_e64 s[2:3], 0, v129
	s_nop 0
	v_add_u32_dpp v168, v168, v168 row_shr:2 row_mask:0xf bank_mask:0xf bound_ctrl:1
	s_nop 1
	v_add_u32_dpp v168, v168, v168 row_shr:4 row_mask:0xf bank_mask:0xf bound_ctrl:1
	s_nop 1
	v_add_u32_dpp v168, v168, v168 row_shr:8 row_mask:0xf bank_mask:0xf bound_ctrl:1
	s_nop 1
	v_add_u32_dpp v168, v168, v168 row_bcast:15 row_mask:0xa bank_mask:0xf
	s_nop 1
	v_add_u32_dpp v168, v168, v168 row_bcast:31 row_mask:0xc bank_mask:0xf
	s_nop 0
	v_readlane_b32 s1, v168, 63
	s_nop 1
	v_sub_u32_e32 v168, s1, v168
	v_add_u32_e32 v170, v168, v0
	v_mov_b32_e32 v0, v251
	v_readlane_b32 s1, v170, 0
	s_nop 1
	v_cvt_f32_u32_e32 v0, s1
	v_mul_f32_e32 v0, 0x43800000, v0
	v_div_scale_f32 v171, s[0:1], v169, v169, v0
	v_rcp_f32_e32 v172, v171
	s_nop 0
	v_fma_f32 v173, -v171, v172, 1.0
	v_fmac_f32_e32 v172, v173, v172
	v_div_scale_f32 v173, vcc, v0, v169, v0
	v_mul_f32_e32 v174, v173, v172
	v_fma_f32 v175, -v171, v174, v173
	v_fmac_f32_e32 v174, v175, v172
	v_fma_f32 v171, -v171, v174, v173
	v_div_fmas_f32 v171, v171, v172, v174
	v_div_fixup_f32 v0, v171, v169, v0
	v_cmp_gt_f32_e32 vcc, s52, v0
	v_mul_f32_e32 v169, 0x4f800000, v0
	s_nop 0
	v_cndmask_b32_e32 v169, v0, v169, vcc
	v_sqrt_f32_e32 v171, v169
	s_nop 0
	v_add_u32_e32 v172, -1, v171
	v_fma_f32 v173, -v172, v171, v169
	v_cmp_ge_f32_e64 s[0:1], 0, v173
	v_add_u32_e32 v173, 1, v171
	s_nop 0
	v_cndmask_b32_e64 v172, v171, v172, s[0:1]
	v_fma_f32 v171, -v173, v171, v169
	v_cmp_lt_f32_e64 s[0:1], 0, v171
	s_nop 1
	v_cndmask_b32_e64 v171, v172, v173, s[0:1]
	v_mul_f32_e32 v172, 0x37800000, v171
	v_cndmask_b32_e32 v171, v171, v172, vcc
	v_cmp_class_f32_e32 vcc, v169, v250
	s_nop 1
	v_cndmask_b32_e32 v169, v171, v169, vcc
	v_mov_b32_e32 v171, 0x40400000
	v_fmamk_f32 v171, v169, 0x40400000, v171
	v_sub_f32_e32 v169, v0, v171
	v_max_f32_e32 v169, 0, v169
	v_cvt_i32_f32_e32 v169, v169
	v_add_f32_e32 v0, v0, v171
	v_cvt_i32_f32_e32 v0, v0
	v_cmp_gt_i32_e64 s[0:1], v170, v169
	v_cmp_le_i32_e32 vcc, v168, v169
	s_or_b64 s[0:1], s[2:3], s[0:1]
	s_and_b64 s[2:3], vcc, s[0:1]
	v_cmp_gt_i32_e32 vcc, v170, v0
	v_cmp_le_i32_e64 s[0:1], v168, v0
	s_and_b64 s[0:1], s[0:1], vcc
	v_cndmask_b32_e64 v170, 0, 1, s[2:3]
	v_cmp_ne_u32_e32 vcc, 0, v170
	v_cndmask_b32_e64 v170, 0, 1, s[0:1]
	v_cmp_ne_u32_e64 s[0:1], 0, v170
	s_cbranch_vccz .LBB0_1239
	s_flbit_i32_b64 s2, vcc
	s_sub_i32 s2, 63, s2
	s_cmp_eq_u64 s[0:1], 0
	s_cselect_b32 s4, 1, 0
	s_flbit_i32_b64 s3, s[0:1]
	s_sub_i32 s3, 63, s3
	s_cmp_lg_u32 s4, 0
	s_cselect_b32 s3, s2, s3
	v_and_b32_e32 v1, 31, v129
	v_lshlrev_b32_e32 v1, 2, v1
	v_sub_u32_e32 v1, 0x7c, v1
	s_lshl_b32 s0, s2, 7
	s_lshl_b32 s1, s3, 7
	v_mov_b32_e32 v3, s0
	v_mov_b32_e32 v4, s1
	v_cmp_lt_u32_e32 vcc, 31, v129
	s_nop 1
	v_cndmask_b32_e32 v3, v3, v4, vcc
	v_add3_u32 v1, v3, v1, s57
	ds_read_b32 v5, v1
	v_readlane_b32 s0, v168, s2
	v_readlane_b32 s1, v168, s3
	s_waitcnt lgkmcnt(0)
	v_add_u32_dpp v6, v5, v5 row_shr:1 row_mask:0xf bank_mask:0xf bound_ctrl:1
	s_nop 1
	v_add_u32_dpp v6, v6, v6 row_shr:2 row_mask:0xf bank_mask:0xf bound_ctrl:1
	s_nop 1
	v_add_u32_dpp v6, v6, v6 row_shr:4 row_mask:0xf bank_mask:0xf bound_ctrl:1
	s_nop 1
	v_add_u32_dpp v6, v6, v6 row_shr:8 row_mask:0xf bank_mask:0xf bound_ctrl:1
	s_nop 1
	v_add_u32_dpp v6, v6, v6 row_bcast:15 row_mask:0xa bank_mask:0xf
	v_sub_u32_e32 v7, v6, v5
	v_add_u32_e32 v7, s0, v7
	v_add_u32_e32 v8, s1, v6
	v_cmp_le_i32_e32 vcc, v7, v169
	v_cmp_gt_i32_e64 s[20:21], v8, v0
	s_bcnt1_i32_b32 s0, vcc_lo
	s_ff1_i32_b32 s1, s21
	s_lshl_b32 s2, s2, 5
	s_lshl_b32 s3, s3, 5
	s_sub_i32 s2, s2, s0
	s_add_i32 s2, s2, 32
	s_sub_i32 s3, s3, s1
	s_add_i32 s3, s3, 31
	s_cmp_lg_u32 s4, 0
	s_cselect_b32 s3, 1, s3
	s_max_u32 s3, s3, 1
	v_mov_b32_e32 v2, s2
	v_mov_b32_e32 v168, s3
